# phase 3: half of the workgroups run the attention units before the GLA-local units (load-bound and compute-bound parts overlap across CUs); plus deferred weight conversion helpers
# speedup vs baseline: 1.0202x; 1.0202x over previous
; #define LAS __attribute__((address_space(3)))
; #define FRESH_TID() do { ap = fresh_args(); ws = ap->ws; unsigned m1_ = ~0u; asm volatile("" : "+s"(m1_)); lane = (int)__builtin_amdgcn_mbcnt_hi(m1_, __builtin_amdgcn_mbcnt_lo(m1_, 0u)); asm volatile("" : "+v"(lane)); wave = wave0; tid = wave0 * 64 + lane; } while (0)
; __device__ __forceinline__ void gla_local_unit(LAS unsigned char* lds, GlaPre& R, const bf16_t* proj, const float* alow, const float (&w2)[16], const float bias, ...
;     const int n = u & 31, h = (u >> 5) & 3, b = u >> 7;
;     const int d = tid & 127, ig = tid >> 7;
;     const int fr = lane & 15, fq = lane >> 4;
;     LAS unsigned char* QD = lds; LAS unsigned char* KI = lds + 17408; LAS unsigned char* KET = lds + 34816; LAS unsigned char* VL = lds + 53248;
;     LAS unsigned char* AT = lds + 86016;
;     LAS float* CS = (LAS float*)(lds + 95232); LAS float* ALs = (LAS float*)(lds + 97280);
;     const size_t t0 = (size_t)b * SEQ + 64 * n;
; #pragma unroll
;     for (int it = 0; it < 2; ++it) { const int id = tid + NTHREADS * it, row = id >> 4, ch = id & 15; *(LAS u32x4*)(QD + row * 272 + ch * 16) = R.q[it]; *(LAS u32x4*)(KI + row * 272 + ch * 16) = R.k[it]; }
;     ALs[tid] = R.al0; ALs[512 + tid] = R.al1;
; #pragma unroll
;     for (int it = 0; it < 4; ++it) { const int id = tid + NTHREADS * it, row = id >> 5, ch = id & 31; *(LAS u32x4*)(VL + swz512(row, ch)) = R.v[it]; }
;     __syncthreads();
; template <unsigned MASK, bool ONE>
; __global__ void __launch_bounds__(NTHREADS, 2) fwd_kernel(Args a_unused) {
;     ...
;         if (IN(P + 2, 3)) { FRESH_TID();
;             {
;                 const int hw = (vcu >> 5) & 3, dw = tid & 127; float w2[16];
; #pragma unroll
;                 for (int r = 0; r < 16; ++r) w2[r] = (a.w_alpha2 + (size_t)l * 16 * 512)[r * 512 + hw * 128 + dw];
;                 const float bias = (a.b_alpha2 + (size_t)l * 512)[hw * 128 + dw];
;                 for (int u = vcu; u < NB * 4 * 32; u += G) { GlaPre R; gla_local_issue(R, proj, alow, u, tid);
.LBB0_347:
	s_or_b64 exec, exec, s[0:1]
	s_mov_b32 s100, 0
.Lsw_start:
	v_readlane_b32 s0, v255, 17
	v_readlane_b32 s1, v255, 18
	s_mov_b32 s1, s97
	v_writelane_b32 v255, s0, 17
	s_mov_b32 s2, s38
	s_waitcnt lgkmcnt(0)
	v_writelane_b32 v255, s1, 18
	v_readlane_b32 s0, v253, 0
	v_readlane_b32 s1, v253, 1
	s_barrier
	s_nop 0
	v_mbcnt_lo_u32_b32 v0, s2, 0
	v_mbcnt_hi_u32_b32 v2, s2, v0
	v_readlane_b32 s2, v253, 10
	v_readlane_b32 s3, v253, 11
	s_andn2_b64 vcc, exec, s[2:3]
	s_cmp_lg_u32 s100, 0
	s_cbranch_scc1 .Lsw_a
	v_readlane_b32 s101, v253, 4
	s_nop 1
	s_bitcmp1_b32 s101, 3
	s_cbranch_scc0 .Lsw_a
	s_mov_b32 s100, 1
	s_branch .LBB0_356
.Lsw_a:
	s_cbranch_vccnz .LBB0_356
	s_load_dwordx4 s[4:7], s[0:1], 0x38
	s_load_dwordx2 s[2:3], s[0:1], 0xa0
	v_readlane_b32 s8, v255, 17
	v_readlane_b32 s9, v255, 18
	v_add_u32_e32 v0, s78, v2
	s_lshl_b64 s[0:1], s[8:9], 15
	v_and_b32_e32 v3, 0x7f, v0
	s_waitcnt lgkmcnt(0)
	s_add_u32 s0, s4, s0
	v_readlane_b32 s4, v253, 9
	s_addc_u32 s1, s5, s1
	v_ashrrev_i32_e32 v22, 5, v0
	v_or_b32_e32 v1, s4, v3
	v_lshlrev_b32_e32 v32, 2, v1
	v_lshl_add_u64 v[4:5], s[0:1], 0, v[32:33]
	v_add_co_u32_e32 v6, vcc, s82, v4
	s_movk_i32 s4, 0x2000
	s_nop 0
	v_addc_co_u32_e32 v7, vcc, 0, v5, vcc
	v_add_co_u32_e32 v8, vcc, s4, v4
	s_movk_i32 s4, 0x3000
	s_nop 0
	v_addc_co_u32_e32 v9, vcc, 0, v5, vcc
	v_add_co_u32_e32 v10, vcc, s4, v4
	s_movk_i32 s4, 0x4000
	s_nop 0
	v_addc_co_u32_e32 v11, vcc, 0, v5, vcc
	v_add_co_u32_e32 v12, vcc, s4, v4
	s_movk_i32 s4, 0x5000
	s_nop 0
	v_addc_co_u32_e32 v13, vcc, 0, v5, vcc
	v_add_co_u32_e32 v14, vcc, s4, v4
	s_movk_i32 s4, 0x6000
	s_nop 0
	v_addc_co_u32_e32 v15, vcc, 0, v5, vcc
	v_add_co_u32_e32 v16, vcc, s4, v4
	s_movk_i32 s4, 0x7000
	s_nop 0
	v_addc_co_u32_e32 v17, vcc, 0, v5, vcc
	v_add_co_u32_e32 v4, vcc, s4, v4
	s_lshl_b64 s[4:5], s[8:9], 11
	global_load_dword v46, v[8:9], off offset:-4096
	global_load_dword v47, v[8:9], off
	global_load_dword v48, v[8:9], off offset:2048
	global_load_dword v49, v[12:13], off offset:-4096
	global_load_dword v50, v[12:13], off
	global_load_dword v51, v[12:13], off offset:2048
	global_load_dword v52, v[16:17], off offset:-4096
	global_load_dword v53, v[16:17], off
	global_load_dword v54, v[16:17], off offset:2048
	s_add_u32 s4, s6, s4
	v_addc_co_u32_e32 v5, vcc, 0, v5, vcc
	s_addc_u32 s5, s7, s5
	global_load_dword v55, v32, s[0:1]
	global_load_dword v56, v32, s[0:1] offset:2048
	global_load_dword v57, v[6:7], off offset:2048
	global_load_dword v58, v[10:11], off offset:2048
	global_load_dword v59, v[14:15], off offset:2048
	global_load_dword v60, v[4:5], off
	global_load_dword v61, v32, s[4:5]
	global_load_dword v62, v[4:5], off offset:2048
	v_add_u32_e32 v6, 0x200, v0
	v_lshlrev_b32_e32 v15, 2, v22
	v_ashrrev_i32_e32 v24, 5, v6
	v_and_b32_e32 v13, 31, v2
	v_and_b32_e32 v15, 12, v15
	v_bfe_u32 v30, v22, 2, 2
	v_bitop3_b32 v15, v15, v13, v30 bitop3:0x36
	v_lshlrev_b32_e32 v30, 2, v24
	v_add_u32_e32 v7, 0x400, v0
	v_and_b32_e32 v30, 12, v30
	v_bfe_u32 v31, v24, 2, 2
	v_ashrrev_i32_e32 v26, 5, v7
	v_bitop3_b32 v30, v30, v13, v31 bitop3:0x36
	v_lshl_add_u32 v45, v30, 4, 0
	v_lshlrev_b32_e32 v30, 2, v26
	v_add_u32_e32 v7, 0x600, v0
	v_and_b32_e32 v30, 12, v30
	v_bfe_u32 v31, v26, 2, 2
	v_ashrrev_i32_e32 v28, 5, v7
	v_bitop3_b32 v30, v30, v13, v31 bitop3:0x36
	v_ashrrev_i32_e32 v11, 7, v0
	v_lshlrev_b32_e32 v12, 2, v0
	v_readlane_b32 s4, v254, 49
	v_lshl_add_u32 v76, v30, 4, 0
	v_lshlrev_b32_e32 v30, 2, v28
	v_ashrrev_i32_e32 v18, 4, v0
	v_add_u32_e32 v63, s4, v12
	v_and_b32_e32 v30, 12, v30
	v_bfe_u32 v31, v28, 2, 2
	v_lshl_add_u32 v64, v11, 10, s4
	v_readlane_b32 s4, v254, 50
	s_movk_i32 s16, 0x90
	v_lshlrev_b32_e32 v5, 4, v0
	v_bitop3_b32 v13, v30, v13, v31 bitop3:0x36
	v_add_u32_e32 v65, s4, v12
	v_lshl_add_u32 v66, v3, 2, s4
	v_lshl_add_u32 v12, v3, 1, 0
	v_mad_u32_u24 v79, v3, s16, 0
	v_and_b32_e32 v3, 3, v2
	s_movk_i32 s14, 0xc0
	v_lshlrev_b32_e32 v30, 2, v18
	v_and_b32_e32 v32, 0xf0, v5
	v_and_or_b32 v3, v5, s14, v3
	v_and_b32_e32 v5, 0x1fffff00, v0
	v_and_b32_e32 v30, 60, v30
	v_ashrrev_i32_e32 v20, 4, v6
	v_or3_b32 v5, v5, v30, v3
	v_lshlrev_b32_e32 v30, 3, v5
	v_and_b32_e32 v5, 0x1fffff00, v6
	v_lshlrev_b32_e32 v6, 2, v20
	v_and_b32_e32 v6, 60, v6
	v_ashrrev_i32_e32 v36, 4, v2
	v_or3_b32 v3, v5, v6, v3
	v_and_b32_e32 v7, 15, v2
; __device__ __forceinline__ void gla_local_unit(LAS unsigned char* lds, GlaPre& R, const bf16_t* proj, const float* alow, const float (&w2)[16], const float bias, ...
;     const int n = u & 31, h = (u >> 5) & 3, b = u >> 7;
;     const int d = tid & 127, ig = tid >> 7;
;     const int fr = lane & 15, fq = lane >> 4;
;     LAS unsigned char* QD = lds; LAS unsigned char* KI = lds + 17408; LAS unsigned char* KET = lds + 34816; LAS unsigned char* VL = lds + 53248;
;     LAS unsigned char* AT = lds + 86016;
;     LAS float* CS = (LAS float*)(lds + 95232); LAS float* ALs = (LAS float*)(lds + 97280);
;     const size_t t0 = (size_t)b * SEQ + 64 * n;
; #pragma unroll
;     for (int it = 0; it < 2; ++it) { const int id = tid + NTHREADS * it, row = id >> 4, ch = id & 15; *(LAS u32x4*)(QD + row * 272 + ch * 16) = R.q[it]; *(LAS u32x4*)(KI + row * 272 + ch * 16) = R.k[it]; }
;     ALs[tid] = R.al0; ALs[512 + tid] = R.al1;
; #pragma unroll
;     for (int it = 0; it < 4; ++it) { const int id = tid + NTHREADS * it, row = id >> 5, ch = id & 31; *(LAS u32x4*)(VL + swz512(row, ch)) = R.v[it]; }
;     __syncthreads();
;     if (u_next >= 0) gla_local_issue(R, proj, alow, u_next, tid);
;     float bl[16]; float run = 0.f;
; #pragma unroll
;     for (int ii = 0; ii < 16; ++ii) { float z = bias; const LAS f32x4* ap = (const LAS f32x4*)(ALs + (16 * ig + ii) * 16);
; #pragma unroll
;         for (int r4 = 0; r4 < 4; ++r4) { const f32x4 av = ap[r4]; z = fmaf(av[0], w2[4 * r4], z); z = fmaf(av[1], w2[4 * r4 + 1], z); z = fmaf(av[2], w2[4 * r4 + 2], z); z = fmaf(av[3], w2[4 * r4 + 3], z); }
;         const float la = (fminf(z, 0.f) - __logf(1.0f + __expf(-fabsf(z)))) * 0.0625f; run += la; bl[ii] = run; }
;     CS[ig * 128 + d] = run;
;     __syncthreads();
;     float pre = 0.f, tot = 0.f;
; #pragma unroll
;     for (int g2 = 0; g2 < 4; ++g2) { const float cv = CS[g2 * 128 + d]; tot += cv; pre += (g2 < ig) ? cv : 0.f; }
;     const float qscale = 0.08838834764831845f; const float etot = __expf(tot);
;     unsigned ke[8];
; #pragma unroll
;     for (int ii = 0; ii < 16; ++ii) { const float bb = pre + bl[ii];
;         LAS bf16_t* qp = (LAS bf16_t*)(QD + (16 * ig + ii) * 272 + 2 * d); LAS bf16_t* kp = (LAS bf16_t*)(KI + (16 * ig + ii) * 272 + 2 * d);
;         const float qf_ = bf2f(*qp), kf_ = bf2f(*kp);
;         const float eb = __expf(bb), einv = __builtin_amdgcn_rcpf(eb);
	v_lshlrev_b32_e32 v34, 3, v3
	v_lshlrev_b32_e32 v3, 2, v36
	v_readlane_b32 s14, v253, 12
	s_movk_i32 s15, 0x110
	v_readlane_b32 s31, v254, 51
	v_add_u32_e32 v5, s14, v3
	v_or_b32_e32 v6, s14, v7
	v_readlane_b32 s14, v253, 15
	v_or_b32_e32 v38, 1, v5
	v_or_b32_e32 v39, 2, v5
	v_or_b32_e32 v37, s14, v7
	v_or_b32_e32 v40, 3, v5
	v_mul_lo_u32 v9, v18, s15
	v_mul_lo_u32 v10, v20, s15
	v_mul_lo_u32 v6, v6, s15
	v_mad_u32_u24 v68, v37, s15, 0
	v_lshl_add_u32 v80, v37, 1, s31
	v_cmp_lt_i32_e64 s[14:15], v5, v37
	v_mul_lo_u32 v81, v5, s16
	v_cmp_lt_i32_e64 s[16:17], v38, v37
	v_cmp_lt_i32_e64 s[18:19], v39, v37
	v_cmp_lt_i32_e64 s[20:21], v40, v37
	v_or_b32_e32 v37, 16, v37
	v_cmp_lt_i32_e64 s[22:23], v5, v37
	v_bfe_u32 v5, v2, 2, 2
	v_and_b32_e32 v67, -16, v2
	v_lshl_add_u32 v83, v37, 1, s31
	v_cmp_lt_i32_e64 s[24:25], v38, v37
	v_cmp_lt_i32_e64 s[26:27], v39, v37
	v_cmp_lt_i32_e64 s[28:29], v40, v37
	v_lshl_or_b32 v5, v36, 3, v5
	v_lshrrev_b32_e32 v37, 1, v2
	v_readlane_b32 s30, v253, 18
	v_and_b32_e32 v38, 12, v2
	v_lshlrev_b32_e32 v36, 1, v36
	v_lshlrev_b32_e32 v2, 3, v2
	v_and_or_b32 v37, v37, 1, s30
	v_and_b32_e32 v36, 2, v36
	v_and_b32_e32 v85, 8, v2
	v_add_u32_e32 v2, 0, v85
	v_or_b32_e32 v39, 4, v5
	v_bitop3_b32 v40, v36, v37, v38 bitop3:0x36
	v_lshl_add_u32 v70, v40, 4, v2
	v_lshlrev_b32_e32 v40, 9, v39
	v_bfe_u32 v39, v39, 2, 2
	v_bitop3_b32 v41, v39, v37, v38 bitop3:0x36
	v_lshlrev_b32_e32 v69, 9, v5
	v_lshlrev_b32_e32 v41, 4, v41
	v_add_u32_e32 v5, 36, v5
	v_add3_u32 v84, 0, v41, v40
	v_lshlrev_b32_e32 v41, 9, v5
	v_bfe_u32 v5, v5, 2, 2
	v_bitop3_b32 v42, v5, v37, v38 bitop3:0x36
	v_or_b32_e32 v37, 2, v37
	v_bitop3_b32 v36, v36, v37, v38 bitop3:0x36
	v_lshl_add_u32 v72, v36, 4, v2
	v_bitop3_b32 v2, v39, v37, v38 bitop3:0x36
	v_lshlrev_b32_e32 v2, 4, v2
	v_add3_u32 v87, 0, v2, v40
	v_bitop3_b32 v2, v5, v37, v38 bitop3:0x36
	s_add_u32 s0, s2, 0x30600000
	s_movk_i32 s12, 0x1100
	v_lshlrev_b32_e32 v2, 4, v2
	s_addc_u32 s1, s3, 0
	v_ashrrev_i32_e32 v1, 31, v0
	v_mul_lo_u32 v78, v11, s12
	s_movk_i32 s12, 0x80
	v_add3_u32 v5, 0, v2, v41
	v_lshl_add_u32 v2, v7, 4, v3
	v_lshlrev_b32_e32 v4, 3, v0
	v_lshl_add_u64 v[16:17], s[0:1], 0, v[32:33]
	v_add_u32_e32 v8, 0, v32
	v_cmp_gt_u32_e64 s[12:13], s12, v0
	v_mov_b32_e32 v32, v0
	v_mul_u32_u24_e32 v89, 0x90, v7
	v_ashrrev_i32_e32 v3, 31, v2
	v_add_u32_e32 v7, s31, v67
	v_lshl_add_u64 v[0:1], v[0:1], 2, s[2:3]
	s_mov_b64 s[30:31], 0x300000
	v_lshl_add_u64 v[36:37], v[0:1], 0, s[30:31]
	v_lshl_add_u64 v[0:1], v[2:3], 1, s[2:3]
	s_mov_b64 s[30:31], 0x4ae00000
	s_add_u32 s36, s2, 0x47e00000
	v_lshlrev_b32_e32 v42, 4, v42
	v_lshl_add_u64 v[38:39], v[0:1], 0, s[30:31]
	s_mov_b64 s[30:31], 0x48e00000
	s_addc_u32 s37, s3, 0
	v_add3_u32 v86, 0, v42, v41
	v_lshl_add_u64 v[40:41], v[0:1], 0, s[30:31]
	v_readlane_b32 s30, v254, 27
	s_add_u32 s2, s2, s30
	v_readlane_b32 s30, v254, 28
	v_and_b32_e32 v4, 0xf8, v4
	v_lshlrev_b32_e32 v14, 9, v22
	v_lshl_add_u32 v15, v15, 4, 0
	v_lshlrev_b32_e32 v44, 9, v24
	v_lshlrev_b32_e32 v75, 9, v26
	v_lshlrev_b32_e32 v77, 9, v28
	v_lshl_add_u32 v13, v13, 4, 0
	v_cmp_lt_i32_e64 s[4:5], 0, v11
	v_cmp_lt_i32_e64 s[6:7], 1, v11
	v_cmp_lt_i32_e64 s[8:9], 2, v11
	v_cmp_lt_i32_e64 s[10:11], 3, v11
	v_lshlrev_b32_e32 v11, 5, v11
	v_add_u32_e32 v6, 0, v6
	v_add_u32_e32 v82, 0x1100, v68
	v_add_u32_e32 v88, 0, v67
	s_addc_u32 s3, s3, s30
	v_ashrrev_i32_e32 v19, 31, v18
	v_ashrrev_i32_e32 v21, 31, v20
	v_ashrrev_i32_e32 v23, 31, v22
	v_ashrrev_i32_e32 v25, 31, v24
	v_ashrrev_i32_e32 v27, 31, v26
	v_ashrrev_i32_e32 v29, 31, v28
	v_ashrrev_i32_e32 v31, 31, v30
	v_ashrrev_i32_e32 v35, 31, v34
	v_add_u32_e32 v71, 0x4000, v69
	v_lshl_add_u64 v[42:43], v[32:33], 2, s[2:3]
	v_lshlrev_b32_e32 v32, 1, v4
	v_add_u32_e32 v73, v15, v14
	v_add_u32_e32 v74, v45, v44
	v_add_u32_e32 v75, v76, v75
	v_add_u32_e32 v76, v13, v77
	v_add_u32_e32 v77, v12, v78
	v_add_u32_e32 v78, v79, v11
	v_add_u32_e32 v79, v80, v81
	v_add_u32_e32 v80, v82, v67
	v_add_u32_e32 v81, v83, v81
	v_add_u32_e32 v82, v84, v85
	v_add_u32_e32 v83, v86, v85
	v_add_u32_e32 v84, v87, v85
	v_add_u32_e32 v85, v5, v85
	v_add_u32_e32 v86, v88, v89
	v_add_u32_e32 v87, v7, v89
	v_add_u32_e32 v88, v8, v9
	v_add_u32_e32 v89, v8, v10
	v_add_u32_e32 v90, v6, v67
	v_readlane_b32 s40, v254, 21
	s_mov_b32 s41, s76
	s_branch .LBB0_350

; #define LAS __attribute__((address_space(3)))
; #define FRESH_TID() do { ap = fresh_args(); ws = ap->ws; unsigned m1_ = ~0u; asm volatile("" : "+s"(m1_)); lane = (int)__builtin_amdgcn_mbcnt_hi(m1_, __builtin_amdgcn_mbcnt_lo(m1_, 0u)); asm volatile("" : "+v"(lane)); wave = wave0; tid = wave0 * 64 + lane; } while (0)
; __device__ __forceinline__ void attn_unit(LAS unsigned char* lds, AttnPre& R, const bf16_t* proj, bf16_t* atto, float* lse, int a, int a_next, int tid, int wave, int lane) {
;     ...
;     { const int fK = ((fr & 3) << 2) | ((fr >> 2) & 3);
; #pragma unroll
;         for (int ks = 0; ks < 4; ++ks) kbase[ks] = (unsigned)(256 * (16 * wave + fr) + 16 * ((4 * ks + fq) ^ fK)); }
; #pragma unroll
;     for (int kt = 0; kt < 9; ++kt) { f32x4 acc = (f32x4){0.f, 0.f, 0.f, 0.f};
; #pragma unroll
;         for (int ks = 0; ks < 4; ++ks) { const bf16x8 kf = *(const LAS bf16x8*)(Kl + kbase[ks] + 4096 * kt); acc = __builtin_amdgcn_mfma_f32_16x16x32_bf16(kf, qf[ks], acc, 0, 0, 0); }
;         sacc[kt] = acc; }
;     const float sc = 0.12751743082459868f;
;     float mx = -3.0e38f;
; #pragma unroll
;     for (int kt = 0; kt < 9; ++kt)
; #pragma unroll
;         for (int rg = 0; rg < 4; ++rg) { const int jk = 16 * (wave + kt) + 4 * fq + rg; const bool valid = (jk >= qi) && (jk <= qi + 128) && (p0 + jk >= 0);
;             const float s = valid ? sacc[kt][rg] * sc : -3.0e38f; sacc[kt][rg] = s; mx = fmaxf(mx, s); }
; template <unsigned MASK, bool ONE>
; __global__ void __launch_bounds__(NTHREADS, 2) fwd_kernel(Args a_unused) {
;     ...
;             FRESH_TID();
;             for (int u = vcu; u < NB * 12 * 16; u += G) { AttnPre R; attn_issue(R, proj, u, tid, wave, lane); attn_unit(lds, R, proj, atto, lse, u, -1, tid, wave, lane); }
.LBB0_356:
	v_readlane_b32 s0, v253, 0
	v_readlane_b32 s1, v253, 1
	s_mov_b32 s2, s38
	s_nop 0
	v_mbcnt_lo_u32_b32 v0, s2, 0
	v_mbcnt_hi_u32_b32 v1, s2, v0
	v_readlane_b32 s2, v253, 20
	v_readlane_b32 s3, v253, 21
	s_andn2_b64 vcc, exec, s[2:3]
	s_cmp_eq_u32 s100, 2
	s_cbranch_scc1 .LBB0_361
	s_cbranch_vccnz .LBB0_361
	s_load_dwordx2 s[40:41], s[0:1], 0xa0
	v_readlane_b32 s0, v255, 21
	v_ashrrev_i32_e32 v28, 4, v1
	v_and_b32_e32 v29, 3, v1
	v_add_u32_e32 v2, s0, v1
	v_add_u32_e32 v4, 0x200, v2
	v_ashrrev_i32_e32 v59, 4, v4
	v_add_u32_e32 v4, 0x400, v2
	v_ashrrev_i32_e32 v60, 4, v4
	v_add_u32_e32 v4, 0x600, v2
	v_ashrrev_i32_e32 v61, 4, v4
	v_add_u32_e32 v4, 0x800, v2
	v_ashrrev_i32_e32 v62, 4, v4
	v_add_u32_e32 v4, 0xa00, v2
	v_ashrrev_i32_e32 v58, 4, v2
	v_ashrrev_i32_e32 v63, 4, v4
	v_add_u32_e32 v4, 0xc00, v2
	v_add_u32_e32 v2, 0xe00, v2
	v_ashrrev_i32_e32 v65, 4, v2
	v_and_b32_e32 v2, 15, v1
	v_readlane_b32 s0, v253, 22
	v_lshlrev_b32_e32 v29, 2, v29
	v_bfe_u32 v30, v1, 2, 2
	v_or_b32_e32 v66, s0, v2
	v_add_u32_e32 v34, 4, v28
	v_add_u32_e32 v35, 8, v28
	v_add_u32_e32 v36, 12, v28
	s_waitcnt lgkmcnt(0)
	s_add_u32 s6, s40, 0x30600000
	v_ashrrev_i32_e32 v64, 4, v4
	v_lshlrev_b32_e32 v31, 8, v66
	v_bitop3_b32 v32, v29, v28, v30 bitop3:0x36
	v_bitop3_b32 v34, v29, v34, v30 bitop3:0x36
	v_bitop3_b32 v35, v29, v35, v30 bitop3:0x36
	v_bitop3_b32 v29, v29, v36, v30 bitop3:0x36
	v_lshlrev_b32_e32 v52, 2, v28
	s_addc_u32 s7, s41, 0
	v_lshlrev_b32_e32 v5, 2, v58
	v_lshlrev_b32_e32 v8, 2, v59
	v_lshlrev_b32_e32 v11, 2, v60
	v_lshlrev_b32_e32 v14, 2, v61
	v_lshlrev_b32_e32 v17, 2, v62
	v_lshlrev_b32_e32 v20, 2, v63
	v_lshlrev_b32_e32 v23, 2, v64
	v_lshlrev_b32_e32 v26, 2, v65
	v_lshl_add_u32 v32, v32, 4, v31
	v_lshl_add_u32 v34, v34, 4, v31
	v_lshl_add_u32 v35, v35, 4, v31
	v_lshl_add_u32 v29, v29, 4, v31
	v_add_u32_e32 v31, 0x80, v66
	v_add_u32_e32 v67, s0, v52
	s_add_u32 s8, s40, 0x2b600000
	v_and_b32_e32 v5, 12, v5
	v_bfe_u32 v6, v58, 2, 2
	v_and_b32_e32 v8, 12, v8
	v_bfe_u32 v9, v59, 2, 2
	v_and_b32_e32 v11, 12, v11
	v_bfe_u32 v12, v60, 2, 2
	v_and_b32_e32 v14, 12, v14
	v_bfe_u32 v15, v61, 2, 2
	v_and_b32_e32 v17, 12, v17
	v_bfe_u32 v18, v62, 2, 2
	v_and_b32_e32 v20, 12, v20
	v_bfe_u32 v21, v63, 2, 2
	v_and_b32_e32 v23, 12, v23
	v_bfe_u32 v24, v64, 2, 2
	v_and_b32_e32 v26, 12, v26
	v_bfe_u32 v27, v65, 2, 2
	v_cmp_ge_i32_e32 vcc, v52, v2
	v_cmp_le_i32_e64 s[4:5], v67, v31
	s_addc_u32 s9, s41, 0
	v_bitop3_b32 v5, v5, v2, v6 bitop3:0x36
	v_bitop3_b32 v8, v8, v2, v9 bitop3:0x36
	v_bitop3_b32 v11, v11, v2, v12 bitop3:0x36
	v_bitop3_b32 v14, v14, v2, v15 bitop3:0x36
	v_bitop3_b32 v17, v17, v2, v18 bitop3:0x36
	v_bitop3_b32 v20, v20, v2, v21 bitop3:0x36
	v_bitop3_b32 v23, v23, v2, v24 bitop3:0x36
	v_bitop3_b32 v26, v26, v2, v27 bitop3:0x36
	s_and_b64 s[0:1], vcc, s[4:5]
	v_or_b32_e32 v2, 1, v67
	v_writelane_b32 v255, s0, 29
	v_cmp_ge_i32_e32 vcc, v2, v66
	v_cmp_lt_i32_e64 s[4:5], v67, v31
	v_writelane_b32 v255, s1, 30
	s_and_b64 s[0:1], vcc, s[4:5]
	v_or_b32_e32 v68, 2, v67
	v_writelane_b32 v255, s0, 31
	v_cmp_ge_i32_e32 vcc, v68, v66
	v_cmp_le_i32_e64 s[4:5], v68, v31
	v_writelane_b32 v255, s1, 32
	s_and_b64 s[0:1], vcc, s[4:5]
	v_or_b32_e32 v69, 3, v67
	v_writelane_b32 v255, s0, 33
	v_cmp_ge_i32_e32 vcc, v69, v66
	v_cmp_le_i32_e64 s[4:5], v69, v31
	v_writelane_b32 v255, s1, 34
	s_and_b64 s[0:1], vcc, s[4:5]
	v_add_u32_e32 v70, 16, v67
	v_writelane_b32 v255, s0, 35
	v_cmp_ge_i32_e32 vcc, v70, v66
	v_cmp_le_i32_e64 s[4:5], v70, v31
	v_writelane_b32 v255, s1, 36
	s_and_b64 s[0:1], vcc, s[4:5]
	v_add_u32_e32 v2, 17, v67
	v_writelane_b32 v255, s0, 37
	v_cmp_ge_i32_e32 vcc, v2, v66
	v_cmp_lt_i32_e64 s[4:5], v70, v31
	v_writelane_b32 v255, s1, 38
	s_and_b64 s[0:1], vcc, s[4:5]
	v_or_b32_e32 v71, 2, v70
	v_writelane_b32 v255, s0, 39
	v_cmp_ge_i32_e32 vcc, v71, v66
	v_cmp_le_i32_e64 s[4:5], v71, v31
	v_or_b32_e32 v72, 3, v70
	v_writelane_b32 v255, s1, 40
	s_and_b64 s[0:1], vcc, s[4:5]
	v_cmp_ge_i32_e32 vcc, v72, v66
	v_cmp_le_i32_e64 s[4:5], v72, v31
	v_add_u32_e32 v73, 32, v67
	s_and_b64 s[24:25], vcc, s[4:5]
	v_cmp_ge_i32_e32 vcc, v73, v66
	v_cmp_le_i32_e64 s[4:5], v73, v31
	v_add_u32_e32 v2, 33, v67
	s_and_b64 s[26:27], vcc, s[4:5]
	v_cmp_ge_i32_e32 vcc, v2, v66
	v_cmp_lt_i32_e64 s[4:5], v73, v31
	v_or_b32_e32 v74, 2, v73
	s_and_b64 s[28:29], vcc, s[4:5]
	v_cmp_ge_i32_e32 vcc, v74, v66
	v_cmp_le_i32_e64 s[4:5], v74, v31
	v_or_b32_e32 v75, 3, v73
	s_and_b64 s[34:35], vcc, s[4:5]
	v_cmp_ge_i32_e32 vcc, v75, v66
	v_cmp_le_i32_e64 s[4:5], v75, v31
	v_add_u32_e32 v76, 48, v67
	s_and_b64 s[36:37], vcc, s[4:5]
	v_cmp_ge_i32_e32 vcc, v76, v66
	v_cmp_le_i32_e64 s[4:5], v76, v31
	v_add_u32_e32 v2, 49, v67
	s_and_b64 s[12:13], vcc, s[4:5]
	v_cmp_ge_i32_e32 vcc, v2, v66
	v_cmp_lt_i32_e64 s[4:5], v76, v31
	v_or_b32_e32 v77, 2, v76
	s_and_b64 s[42:43], vcc, s[4:5]
	v_cmp_ge_i32_e32 vcc, v77, v66
	v_cmp_le_i32_e64 s[4:5], v77, v31
	v_or_b32_e32 v78, 3, v76
	s_and_b64 s[68:69], vcc, s[4:5]
	v_cmp_ge_i32_e32 vcc, v78, v66
	v_cmp_le_i32_e64 s[4:5], v78, v31
	v_add_u32_e32 v79, 64, v67
	s_and_b64 s[44:45], vcc, s[4:5]
	v_cmp_ge_i32_e32 vcc, v79, v66
	v_cmp_le_i32_e64 s[4:5], v79, v31
	v_add_u32_e32 v2, 0x41, v67
	s_and_b64 s[20:21], vcc, s[4:5]
	v_cmp_ge_i32_e32 vcc, v2, v66
	v_cmp_lt_i32_e64 s[4:5], v79, v31
	v_or_b32_e32 v80, 2, v79
	s_and_b64 s[30:31], vcc, s[4:5]
; #define LAS __attribute__((address_space(3)))
; __device__ __forceinline__ void attn_unit(LAS unsigned char* lds, AttnPre& R, const bf16_t* proj, bf16_t* atto, float* lse, int a, int a_next, int tid, int wave, int lane) {
;     ...
;     { const int fK = ((fr & 3) << 2) | ((fr >> 2) & 3);
; #pragma unroll
;         for (int ks = 0; ks < 4; ++ks) kbase[ks] = (unsigned)(256 * (16 * wave + fr) + 16 * ((4 * ks + fq) ^ fK)); }
; #pragma unroll
;     for (int kt = 0; kt < 9; ++kt) { f32x4 acc = (f32x4){0.f, 0.f, 0.f, 0.f};
; #pragma unroll
;         for (int ks = 0; ks < 4; ++ks) { const bf16x8 kf = *(const LAS bf16x8*)(Kl + kbase[ks] + 4096 * kt); acc = __builtin_amdgcn_mfma_f32_16x16x32_bf16(kf, qf[ks], acc, 0, 0, 0); }
;         sacc[kt] = acc; }
;     const float sc = 0.12751743082459868f;
;     float mx = -3.0e38f;
; #pragma unroll
;     for (int kt = 0; kt < 9; ++kt)
; #pragma unroll
;         for (int rg = 0; rg < 4; ++rg) { const int jk = 16 * (wave + kt) + 4 * fq + rg; const bool valid = (jk >= qi) && (jk <= qi + 128) && (p0 + jk >= 0);
;             const float s = valid ? sacc[kt][rg] * sc : -3.0e38f; sacc[kt][rg] = s; mx = fmaxf(mx, s); }
;     mx = fmaxf(mx, sx<16>(mx, lane)); mx = fmaxf(mx, sx<32>(mx, lane));
;     float sum = 0.f;
; #pragma unroll
;     for (int kt = 0; kt < 9; ++kt)
; #pragma unroll
;         for (int rg = 0; rg < 4; ++rg) { const float p = __builtin_amdgcn_exp2f(sacc[kt][rg] - mx); sacc[kt][rg] = p; sum += p; }
;     sum += sx<16>(sum, lane); sum += sx<32>(sum, lane);
; #pragma unroll
;     for (int it = 0; it < 8; ++it) { const int id = tid + NTHREADS * it, row = id >> 4, ch = id & 15; *(LAS u32x4*)(Vl + swz256(row, ch)) = vv[it]; }
;     __syncthreads();
;     if (a_next >= 0) attn_issue(R, proj, a_next, tid, wave, lane);
;     f32x4 oacc[8];
; #pragma unroll
;     for (int dt = 0; dt < 8; ++dt) oacc[dt] = (f32x4){0.f, 0.f, 0.f, 0.f};
;     const int li = lane & 15, qq = li >> 2, pp = li & 3;
;     unsigned vbase[8];
;     { const int fV = (qq << 2) | fq;
; #pragma unroll
;         for (int dt = 0; dt < 8; ++dt) vbase[dt] = (unsigned)(256 * (16 * wave + 4 * fq + qq) + 16 * ((2 * dt + (pp >> 1)) ^ fV) + 8 * (pp & 1)); }
	v_cmp_ge_i32_e32 vcc, v80, v66
	v_cmp_le_i32_e64 s[4:5], v80, v31
	v_or_b32_e32 v81, 3, v79
	s_and_b64 s[76:77], vcc, s[4:5]
	v_cmp_ge_i32_e32 vcc, v81, v66
	v_cmp_le_i32_e64 s[4:5], v81, v31
	v_add_u32_e32 v82, 0x50, v67
	s_and_b64 s[54:55], vcc, s[4:5]
	v_cmp_ge_i32_e32 vcc, v82, v66
	v_cmp_le_i32_e64 s[4:5], v82, v31
	v_add_u32_e32 v2, 0x51, v67
	s_and_b64 s[56:57], vcc, s[4:5]
	v_cmp_ge_i32_e32 vcc, v2, v66
	v_cmp_lt_i32_e64 s[4:5], v82, v31
	v_or_b32_e32 v83, 2, v82
	s_and_b64 s[22:23], vcc, s[4:5]
	v_cmp_ge_i32_e32 vcc, v83, v66
	v_cmp_le_i32_e64 s[4:5], v83, v31
	v_or_b32_e32 v84, 3, v82
	s_and_b64 s[64:65], vcc, s[4:5]
	v_cmp_ge_i32_e32 vcc, v84, v66
	v_cmp_le_i32_e64 s[4:5], v84, v31
	v_add_u32_e32 v85, 0x60, v67
	s_and_b64 s[78:79], vcc, s[4:5]
	v_cmp_ge_i32_e32 vcc, v85, v66
	v_cmp_le_i32_e64 s[4:5], v85, v31
	v_add_u32_e32 v2, 0x61, v67
	s_and_b64 s[52:53], vcc, s[4:5]
	v_cmp_ge_i32_e32 vcc, v2, v66
	v_cmp_lt_i32_e64 s[4:5], v85, v31
	v_or_b32_e32 v86, 2, v85
	s_and_b64 s[72:73], vcc, s[4:5]
	v_cmp_ge_i32_e32 vcc, v86, v66
	v_cmp_le_i32_e64 s[4:5], v86, v31
	v_or_b32_e32 v87, 3, v85
	s_and_b64 s[88:89], vcc, s[4:5]
	v_cmp_ge_i32_e32 vcc, v87, v66
	v_cmp_le_i32_e64 s[4:5], v87, v31
	v_add_u32_e32 v88, 0x70, v67
	s_and_b64 s[92:93], vcc, s[4:5]
	v_cmp_ge_i32_e32 vcc, v88, v66
	v_cmp_le_i32_e64 s[4:5], v88, v31
	v_add_u32_e32 v2, 0x71, v67
	s_and_b64 s[90:91], vcc, s[4:5]
	v_cmp_ge_i32_e32 vcc, v2, v66
	v_cmp_lt_i32_e64 s[4:5], v88, v31
	v_or_b32_e32 v89, 2, v88
	s_and_b64 s[94:95], vcc, s[4:5]
	v_cmp_ge_i32_e32 vcc, v89, v66
	v_cmp_le_i32_e64 s[4:5], v89, v31
	v_or_b32_e32 v90, 3, v88
	s_and_b64 s[66:67], vcc, s[4:5]
	v_cmp_ge_i32_e32 vcc, v90, v66
	v_cmp_le_i32_e64 s[4:5], v90, v31
	v_add_u32_e32 v91, 0x80, v67
	s_and_b64 s[46:47], vcc, s[4:5]
	v_cmp_ge_i32_e32 vcc, v91, v66
	v_cmp_le_i32_e64 s[4:5], v91, v31
	v_add_u32_e32 v2, 0x81, v67
	s_and_b64 s[86:87], vcc, s[4:5]
	v_cmp_ge_i32_e32 vcc, v2, v66
	v_cmp_lt_i32_e64 s[4:5], v91, v31
	v_or_b32_e32 v92, 2, v91
	s_and_b64 s[18:19], vcc, s[4:5]
	v_cmp_ge_i32_e32 vcc, v92, v66
	v_cmp_le_i32_e64 s[4:5], v92, v31
	v_or_b32_e32 v93, 3, v91
	v_writelane_b32 v255, s0, 41
	s_and_b64 s[2:3], vcc, s[4:5]
	v_cmp_ge_i32_e32 vcc, v93, v66
	v_cmp_le_i32_e64 s[4:5], v93, v31
	v_writelane_b32 v255, s1, 42
	s_and_b64 s[0:1], vcc, s[4:5]
	s_add_i32 s4, 0, 0x10000
	v_lshlrev_b32_e32 v5, 4, v5
	v_lshlrev_b32_e32 v8, 4, v8
	v_lshlrev_b32_e32 v11, 4, v11
	v_lshlrev_b32_e32 v14, 4, v14
	v_lshlrev_b32_e32 v17, 4, v17
	v_lshlrev_b32_e32 v20, 4, v20
	v_lshlrev_b32_e32 v23, 4, v23
	v_lshlrev_b32_e32 v26, 4, v26
	v_lshlrev_b32_e32 v2, 2, v1
	s_add_u32 s10, s40, 0x400000
	v_lshlrev_b32_e32 v3, 3, v1
	v_add_u32_e32 v6, 0, v5
	v_add_u32_e32 v9, 0, v8
	v_add_u32_e32 v12, 0, v11
	v_add_u32_e32 v15, 0, v14
	v_add_u32_e32 v18, 0, v17
	v_add_u32_e32 v21, 0, v20
	v_add_u32_e32 v24, 0, v23
	v_add_u32_e32 v27, 0, v26
	v_xor_b32_e32 v94, 0x80, v2
	v_add_u32_e32 v2, s4, v5
	v_add_u32_e32 v5, s4, v8
	v_add_u32_e32 v8, s4, v11
	v_add_u32_e32 v11, s4, v14
	v_add_u32_e32 v14, s4, v17
	v_add_u32_e32 v17, s4, v20
	v_add_u32_e32 v20, s4, v23
	v_add_u32_e32 v23, s4, v26
	v_and_b32_e32 v26, 12, v1
	s_addc_u32 s11, s41, 0
	v_and_b32_e32 v0, 0x78, v3
	v_or_b32_e32 v31, v26, v28
	v_or_b32_e32 v30, v67, v30
	v_bfe_u32 v36, v1, 1, 1
	v_and_b32_e32 v3, 8, v3
	v_writelane_b32 v255, s10, 43
	v_ashrrev_i32_e32 v4, 1, v1
	v_lshl_or_b32 v3, v30, 8, v3
	v_bitop3_b32 v26, v36, v26, v28 bitop3:0x1e
	v_bitop3_b32 v28, v36, v31, 2 bitop3:0x36
	v_bitop3_b32 v30, v36, v31, 4 bitop3:0x36
	v_bitop3_b32 v37, v36, v31, 6 bitop3:0x36
	v_bitop3_b32 v38, v36, v31, 8 bitop3:0x36
	v_bitop3_b32 v39, v36, v31, 10 bitop3:0x36
	v_bitop3_b32 v40, v36, v31, 12 bitop3:0x36
	v_bitop3_b32 v31, v36, v31, 14 bitop3:0x36
	v_writelane_b32 v255, s11, 44
	v_and_b32_e32 v50, -8, v4
	v_lshlrev_b32_e32 v4, 8, v58
	v_lshlrev_b32_e32 v7, 8, v59
	v_lshlrev_b32_e32 v10, 8, v60
	v_lshlrev_b32_e32 v13, 8, v61
	v_lshlrev_b32_e32 v16, 8, v62
	v_lshlrev_b32_e32 v19, 8, v63
	v_lshlrev_b32_e32 v22, 8, v64
	v_lshlrev_b32_e32 v25, 8, v65
	v_lshl_add_u32 v26, v26, 4, s4
	v_lshl_add_u32 v28, v28, 4, s4
	v_lshl_add_u32 v30, v30, 4, s4
	v_lshl_add_u32 v36, v37, 4, s4
	v_lshl_add_u32 v37, v38, 4, s4
	v_lshl_add_u32 v38, v39, 4, s4
	v_lshl_add_u32 v39, v40, 4, s4
	v_lshl_add_u32 v31, v31, 4, s4
	v_readlane_b32 s10, v255, 19
	v_ashrrev_i32_e32 v51, 31, v50
	v_ashrrev_i32_e32 v53, 31, v52
	v_cmp_gt_u32_e64 s[4:5], 16, v1
	v_lshlrev_b32_e32 v54, 1, v0
	v_add_u32_e32 v95, v6, v4
	v_add_u32_e32 v96, v9, v7
	v_add_u32_e32 v97, v12, v10
	v_add_u32_e32 v98, v15, v13
	v_add_u32_e32 v99, v18, v16
	v_add_u32_e32 v100, v21, v19
	v_add_u32_e32 v101, v24, v22
	v_add_u32_e32 v102, v27, v25
	v_add_u32_e32 v103, 0, v32
	v_add_u32_e32 v104, 0, v34
	v_add_u32_e32 v105, 0, v35
	v_add_u32_e32 v106, 0, v29
	v_add_u32_e32 v107, v2, v4
	v_add_u32_e32 v108, v5, v7
	v_add_u32_e32 v109, v8, v10
	v_add_u32_e32 v110, v11, v13
	v_add_u32_e32 v111, v14, v16
	v_add_u32_e32 v112, v17, v19
	v_add_u32_e32 v113, v20, v22
	v_add_u32_e32 v114, v23, v25
	v_add_u32_e32 v115, v26, v3
	v_add_u32_e32 v116, v28, v3
	v_add_u32_e32 v117, v30, v3
	v_add_u32_e32 v118, v36, v3
	v_add_u32_e32 v119, v37, v3
	v_add_u32_e32 v120, v38, v3
	v_add_u32_e32 v121, v39, v3
	v_add_u32_e32 v122, v31, v3
	s_mov_b32 s71, s10
	v_readlane_b32 s11, v255, 20
	s_branch .LBB0_359

; #define FRESH_TID() do { ap = fresh_args(); ws = ap->ws; unsigned m1_ = ~0u; asm volatile("" : "+s"(m1_)); lane = (int)__builtin_amdgcn_mbcnt_hi(m1_, __builtin_amdgcn_mbcnt_lo(m1_, 0u)); asm volatile("" : "+v"(lane)); wave = wave0; tid = wave0 * 64 + lane; } while (0)
; template <unsigned MASK, bool ONE>
; __global__ void __launch_bounds__(NTHREADS, 2) fwd_kernel(Args a_unused) {
;     ...
;             FRESH_TID();
;             for (int u = vcu; u < NB * 12 * 16; u += G) { AttnPre R; attn_issue(R, proj, u, tid, wave, lane); attn_unit(lds, R, proj, atto, lse, u, -1, tid, wave, lane); }
;     ...
;             for (int u = vcu; u < NB * 12 * 16; u += G) { AttnPre R; attn_issue(R, proj, u, tid, wave, lane); attn_unit(lds, R, proj, atto, lse, u, -1, tid, wave, lane); }
;     ...
;         }
.LBB0_361:
	s_cmp_eq_u32 s100, 1
	s_cbranch_scc0 .Lsw_done
	s_mov_b32 s100, 2
	v_readlane_b32 s76, v255, 19
	v_readlane_b32 s78, v255, 21
	s_waitcnt vmcnt(0) lgkmcnt(0)
	s_barrier
	s_branch .Lsw_start
